# GDN chain loader: counted vmcnt(20) instead of vmcnt(0) drains (3-stage prefetch kept in flight)
# speedup vs baseline: 1.3287x; 1.3287x over previous
; #define LDS_BARRIER() asm volatile("s_waitcnt lgkmcnt(0)\n\ts_barrier" ::: "memory")
; __device__ void phase_gdn_chain(const Params& p, int l, char* smem, int vb, int nvb, int oz) {
;     ...
;             for (int ci = 0; ci < 36; ci += 6) {
;                 GDN_FILL(rb, vb_, gb, 1)  if (ci + 4 < 36) GDN_LOAD(rb, vb_, gb, ci + 4)  LDS_BARRIER();
;                 GDN_FILL(rc, vc_, gc, 0)  if (ci + 5 < 36) GDN_LOAD(rc, vc_, gc, ci + 5)  LDS_BARRIER();
;                 GDN_FILL(ra, va, ga, 1)  if (ci + 6 < 36) GDN_LOAD(ra, va, ga, ci + 6)  LDS_BARRIER();
;                 GDN_FILL(rb, vb_, gb, 0)  if (ci + 7 < 36) GDN_LOAD(rb, vb_, gb, ci + 7)  LDS_BARRIER();
;                 GDN_FILL(rc, vc_, gc, 1)  if (ci + 8 < 36) GDN_LOAD(rc, vc_, gc, ci + 8)  LDS_BARRIER();
;                 if (ci + 6 < 36) GDN_FILL(ra, va, ga, 0)  if (ci + 9 < 36) GDN_LOAD(ra, va, ga, ci + 9)  LDS_BARRIER();
.LBB0_442:
	v_add_u32_e32 v224, 0x11e10, v223
	v_add_u32_e32 v225, 0x14210, v193
	s_waitcnt vmcnt(20)
	ds_write_b128 v223, v[68:71] offset:45584
	ds_write_b128 v223, v[96:99] offset:50192
	ds_write_b128 v223, v[72:75] offset:54800
	ds_write_b128 v223, v[76:79] offset:59408
	ds_write_b128 v223, v[88:91] offset:64016
	ds_write_b128 v214, v[80:83] offset:64016
	ds_write_b128 v224, v[84:87]
	ds_write_b128 v224, v[104:107] offset:4608
	ds_write_b128 v225, v[92:95]
	ds_write_b128 v225, v[100:103] offset:4096
	s_and_saveexec_b64 s[42:43], s[38:39]
	ds_write_b32 v195, v220
	s_or_b64 exec, exec, s[42:43]
	s_and_saveexec_b64 s[42:43], s[40:41]
	s_cbranch_execz .LBB0_446
	v_readlane_b32 s17, v255, 40
	s_nop 1
	v_mov_b32_e32 v68, s17
	ds_write_b32 v68, v219

; #define LDS_BARRIER() asm volatile("s_waitcnt lgkmcnt(0)\n\ts_barrier" ::: "memory")
; __device__ void phase_gdn_chain(const Params& p, int l, char* smem, int vb, int nvb, int oz) {
;     ...
;             for (int ci = 0; ci < 36; ci += 6) {
;                 GDN_FILL(rb, vb_, gb, 1)  if (ci + 4 < 36) GDN_LOAD(rb, vb_, gb, ci + 4)  LDS_BARRIER();
;                 GDN_FILL(rc, vc_, gc, 0)  if (ci + 5 < 36) GDN_LOAD(rc, vc_, gc, ci + 5)  LDS_BARRIER();
;                 GDN_FILL(ra, va, ga, 1)  if (ci + 6 < 36) GDN_LOAD(ra, va, ga, ci + 6)  LDS_BARRIER();
;                 GDN_FILL(rb, vb_, gb, 0)  if (ci + 7 < 36) GDN_LOAD(rb, vb_, gb, ci + 7)  LDS_BARRIER();
;                 GDN_FILL(rc, vc_, gc, 1)  if (ci + 8 < 36) GDN_LOAD(rc, vc_, gc, ci + 8)  LDS_BARRIER();
;                 if (ci + 6 < 36) GDN_FILL(ra, va, ga, 0)  if (ci + 9 < 36) GDN_LOAD(ra, va, ga, ci + 9)  LDS_BARRIER();
.LBB0_450:
	s_or_b64 exec, exec, s[46:47]
	s_waitcnt lgkmcnt(0)
	s_barrier
	s_waitcnt vmcnt(20)
	ds_write_b128 v223, v[108:111]
	ds_write_b128 v223, v[136:139] offset:4608
	ds_write_b128 v223, v[112:115] offset:9216
	ds_write_b128 v223, v[116:119] offset:13824
	ds_write_b128 v223, v[124:127] offset:18432
	ds_write_b128 v223, v[120:123] offset:23040
	ds_write_b128 v223, v[128:131] offset:27648
	ds_write_b128 v223, v[140:143] offset:32256
	ds_write_b128 v193, v[132:135] offset:36864
	ds_write_b128 v193, v[144:147] offset:40960
	s_and_saveexec_b64 s[42:43], s[38:39]
	ds_write_b32 v213, v222 offset:45056
	s_or_b64 exec, exec, s[42:43]
	s_and_saveexec_b64 s[42:43], s[40:41]
	ds_write_b32 v3, v221 offset:45568
	s_or_b64 exec, exec, s[42:43]
	s_add_i32 s25, s3, -4
	s_add_i32 s31, s24, 4
	s_and_b64 s[26:27], s[44:45], exec
	s_cselect_b32 s25, s25, s31
	s_add_i32 s26, s25, s2
	s_ashr_i32 s27, s26, 31
	s_add_u32 s42, s26, s84
	s_addc_u32 s43, s27, 0
	s_lshl_b64 s[46:47], s[42:43], 13
	s_add_u32 s48, s4, s46
	s_addc_u32 s49, s5, s47
	s_add_u32 s50, s6, s46
	s_addc_u32 s51, s7, s47
	s_lshl_b64 s[26:27], s[26:27], 13
	s_add_u32 s52, s8, s26
	s_addc_u32 s53, s9, s27
	s_add_u32 s26, s10, s26
	s_addc_u32 s27, s11, s27
	s_add_u32 s46, s12, s46
	s_addc_u32 s47, s13, s47
	global_load_dwordx4 v[108:111], v2, s[48:49]
	global_load_dwordx4 v[112:115], v2, s[50:51]
	global_load_dwordx4 v[116:119], v215, s[50:51]
	global_load_dwordx4 v[120:123], v215, s[52:53]
	global_load_dwordx4 v[124:127], v2, s[52:53]
	global_load_dwordx4 v[128:131], v2, s[26:27]
	global_load_dwordx4 v[136:139], v215, s[48:49]
	global_load_dwordx4 v[132:135], v2, s[46:47]
	global_load_dwordx4 v[140:143], v215, s[26:27]
	global_load_dwordx4 v[144:147], v215, s[46:47]
	s_lshl_b64 s[26:27], s[42:43], 10
	s_add_u32 s42, s14, s26
	s_addc_u32 s43, s15, s27
	s_and_saveexec_b64 s[46:47], s[38:39]
	s_cbranch_execz .LBB0_456
	global_load_dword v222, v216, s[42:43]

; #define LDS_BARRIER() asm volatile("s_waitcnt lgkmcnt(0)\n\ts_barrier" ::: "memory")
; __device__ void phase_gdn_chain(const Params& p, int l, char* smem, int vb, int nvb, int oz) {
;     ...
;             for (int ci = 0; ci < 36; ci += 6) {
;                 GDN_FILL(rb, vb_, gb, 1)  if (ci + 4 < 36) GDN_LOAD(rb, vb_, gb, ci + 4)  LDS_BARRIER();
;                 GDN_FILL(rc, vc_, gc, 0)  if (ci + 5 < 36) GDN_LOAD(rc, vc_, gc, ci + 5)  LDS_BARRIER();
;                 GDN_FILL(ra, va, ga, 1)  if (ci + 6 < 36) GDN_LOAD(ra, va, ga, ci + 6)  LDS_BARRIER();
;                 GDN_FILL(rb, vb_, gb, 0)  if (ci + 7 < 36) GDN_LOAD(rb, vb_, gb, ci + 7)  LDS_BARRIER();
;                 GDN_FILL(rc, vc_, gc, 1)  if (ci + 8 < 36) GDN_LOAD(rc, vc_, gc, ci + 8)  LDS_BARRIER();
;                 if (ci + 6 < 36) GDN_FILL(ra, va, ga, 0)  if (ci + 9 < 36) GDN_LOAD(ra, va, ga, ci + 9)  LDS_BARRIER();
.LBB0_458:
	s_or_b64 exec, exec, s[46:47]
	s_waitcnt lgkmcnt(0)
	s_barrier
	s_waitcnt vmcnt(20)
	ds_write_b128 v223, v[148:151] offset:45584
	ds_write_b128 v223, v[172:175] offset:50192
	ds_write_b128 v223, v[152:155] offset:54800
	ds_write_b128 v223, v[156:159] offset:59408
	ds_write_b128 v223, v[164:167] offset:64016
	ds_write_b128 v214, v[160:163] offset:64016
	ds_write_b128 v224, v[168:171]
	ds_write_b128 v224, v[180:183] offset:4608
	ds_write_b128 v225, v[176:179]
	ds_write_b128 v225, v[184:187] offset:4096
	s_and_saveexec_b64 s[42:43], s[38:39]
	ds_write_b32 v195, v218
	s_or_b64 exec, exec, s[42:43]
	s_and_saveexec_b64 s[42:43], s[40:41]
	s_cbranch_execz .LBB0_462
	v_readlane_b32 s17, v255, 40
	s_nop 1
	v_mov_b32_e32 v226, s17
	ds_write_b32 v226, v217

; #define LDS_BARRIER() asm volatile("s_waitcnt lgkmcnt(0)\n\ts_barrier" ::: "memory")
; __device__ void phase_gdn_chain(const Params& p, int l, char* smem, int vb, int nvb, int oz) {
;     ...
;             for (int ci = 0; ci < 36; ci += 6) {
;                 GDN_FILL(rb, vb_, gb, 1)  if (ci + 4 < 36) GDN_LOAD(rb, vb_, gb, ci + 4)  LDS_BARRIER();
;                 GDN_FILL(rc, vc_, gc, 0)  if (ci + 5 < 36) GDN_LOAD(rc, vc_, gc, ci + 5)  LDS_BARRIER();
;                 GDN_FILL(ra, va, ga, 1)  if (ci + 6 < 36) GDN_LOAD(ra, va, ga, ci + 6)  LDS_BARRIER();
;                 GDN_FILL(rb, vb_, gb, 0)  if (ci + 7 < 36) GDN_LOAD(rb, vb_, gb, ci + 7)  LDS_BARRIER();
;                 GDN_FILL(rc, vc_, gc, 1)  if (ci + 8 < 36) GDN_LOAD(rc, vc_, gc, ci + 8)  LDS_BARRIER();
;                 if (ci + 6 < 36) GDN_FILL(ra, va, ga, 0)  if (ci + 9 < 36) GDN_LOAD(ra, va, ga, ci + 9)  LDS_BARRIER();
.LBB0_468:
	s_waitcnt lgkmcnt(0)
	s_barrier
	s_cmp_gt_u32 s25, 29
	s_cbranch_scc1 .Lgl_s4_last
	s_waitcnt vmcnt(20)
	s_branch .Lgl_s4_go
.Lgl_s4_last:
	s_waitcnt vmcnt(10)
.Lgl_s4_go:
	ds_write_b128 v223, v[68:71]
	ds_write_b128 v223, v[96:99] offset:4608
	ds_write_b128 v223, v[72:75] offset:9216
	ds_write_b128 v223, v[76:79] offset:13824
	ds_write_b128 v223, v[88:91] offset:18432
	ds_write_b128 v223, v[80:83] offset:23040
	ds_write_b128 v223, v[84:87] offset:27648
	ds_write_b128 v223, v[104:107] offset:32256
	ds_write_b128 v193, v[92:95] offset:36864
	ds_write_b128 v193, v[100:103] offset:40960
	s_and_saveexec_b64 s[46:47], s[38:39]
	s_cbranch_execnz .LBB0_471
	s_or_b64 exec, exec, s[46:47]
	s_and_saveexec_b64 s[46:47], s[40:41]
	s_cbranch_execnz .LBB0_472

; #define LDS_BARRIER() asm volatile("s_waitcnt lgkmcnt(0)\n\ts_barrier" ::: "memory")
; __device__ void phase_gdn_chain(const Params& p, int l, char* smem, int vb, int nvb, int oz) {
;     ...
;             for (int ci = 0; ci < 36; ci += 6) {
;                 GDN_FILL(rb, vb_, gb, 1)  if (ci + 4 < 36) GDN_LOAD(rb, vb_, gb, ci + 4)  LDS_BARRIER();
;                 GDN_FILL(rc, vc_, gc, 0)  if (ci + 5 < 36) GDN_LOAD(rc, vc_, gc, ci + 5)  LDS_BARRIER();
;                 GDN_FILL(ra, va, ga, 1)  if (ci + 6 < 36) GDN_LOAD(ra, va, ga, ci + 6)  LDS_BARRIER();
;                 GDN_FILL(rb, vb_, gb, 0)  if (ci + 7 < 36) GDN_LOAD(rb, vb_, gb, ci + 7)  LDS_BARRIER();
;                 GDN_FILL(rc, vc_, gc, 1)  if (ci + 8 < 36) GDN_LOAD(rc, vc_, gc, ci + 8)  LDS_BARRIER();
;                 if (ci + 6 < 36) GDN_FILL(ra, va, ga, 0)  if (ci + 9 < 36) GDN_LOAD(ra, va, ga, ci + 9)  LDS_BARRIER();
.Lgl_s5_go:
	ds_write_b128 v223, v[108:111] offset:45584
	ds_write_b128 v223, v[136:139] offset:50192
	ds_write_b128 v223, v[112:115] offset:54800
	ds_write_b128 v223, v[116:119] offset:59408
	ds_write_b128 v223, v[124:127] offset:64016
	ds_write_b128 v214, v[120:123] offset:64016
	ds_write_b128 v224, v[128:131]
	ds_write_b128 v224, v[140:143] offset:4608
	ds_write_b128 v225, v[132:135]
	ds_write_b128 v225, v[144:147] offset:4096
	s_and_saveexec_b64 s[46:47], s[38:39]
	s_cbranch_execnz .LBB0_481
	s_or_b64 exec, exec, s[46:47]
	s_and_saveexec_b64 s[46:47], s[40:41]
	s_cbranch_execnz .LBB0_482

; #define LDS_BARRIER() asm volatile("s_waitcnt lgkmcnt(0)\n\ts_barrier" ::: "memory")
; __device__ void phase_gdn_chain(const Params& p, int l, char* smem, int vb, int nvb, int oz) {
;     ...
;             for (int ci = 0; ci < 36; ci += 6) {
;                 GDN_FILL(rb, vb_, gb, 1)  if (ci + 4 < 36) GDN_LOAD(rb, vb_, gb, ci + 4)  LDS_BARRIER();
;                 GDN_FILL(rc, vc_, gc, 0)  if (ci + 5 < 36) GDN_LOAD(rc, vc_, gc, ci + 5)  LDS_BARRIER();
;                 GDN_FILL(ra, va, ga, 1)  if (ci + 6 < 36) GDN_LOAD(ra, va, ga, ci + 6)  LDS_BARRIER();
;                 GDN_FILL(rb, vb_, gb, 0)  if (ci + 7 < 36) GDN_LOAD(rb, vb_, gb, ci + 7)  LDS_BARRIER();
;                 GDN_FILL(rc, vc_, gc, 1)  if (ci + 8 < 36) GDN_LOAD(rc, vc_, gc, ci + 8)  LDS_BARRIER();
;                 if (ci + 6 < 36) GDN_FILL(ra, va, ga, 0)  if (ci + 9 < 36) GDN_LOAD(ra, va, ga, ci + 9)  LDS_BARRIER();
.LBB0_488:
	s_waitcnt lgkmcnt(0)
	s_barrier
	s_andn2_b64 vcc, exec, s[42:43]
	s_cbranch_vccnz .LBB0_494
	s_waitcnt vmcnt(20)
	ds_write_b128 v223, v[148:151]
	ds_write_b128 v223, v[172:175] offset:4608
	ds_write_b128 v223, v[152:155] offset:9216
	ds_write_b128 v223, v[156:159] offset:13824
	ds_write_b128 v223, v[164:167] offset:18432
	ds_write_b128 v223, v[160:163] offset:23040
	ds_write_b128 v223, v[168:171] offset:27648
	ds_write_b128 v223, v[180:183] offset:32256
	ds_write_b128 v193, v[176:179] offset:36864
	ds_write_b128 v193, v[184:187] offset:40960
	s_and_saveexec_b64 s[42:43], s[38:39]
	ds_write_b32 v213, v218 offset:45056
	s_or_b64 exec, exec, s[42:43]
	s_and_saveexec_b64 s[42:43], s[40:41]
	ds_write_b32 v3, v217 offset:45568
	s_or_b64 exec, exec, s[42:43]
